# g2p + final RMSNorm row loop software-pipelined (next row's loads issued before the current row's compute and stores)
# baseline (speedup 1.0000x reference)
; __device__ __forceinline__ float wave_sum(float v) { v += dpp_f<0xB1>(v); v += dpp_f<0x4E>(v); v += dpp_f<0x141>(v); v += dpp_f<0x140>(v); return sum_xor32(sum_xor16(v)); }
; __device__ __forceinline__ void final_row(const bf16* hrow, const float* ss, const f32x4 (&gv)[8], float* orow, int lane) {
;     v4u h[4];
; #pragma unroll
;     for (int j = 0; j < 4; ++j) h[j] = *(const v4u*)(hrow + 8 * (lane + 64 * j));
;     const float s = wave_sum((lane < 32) ? ss[lane & 31] : 0.f);
; __global__ void __launch_bounds__(NWAVES * 64, 2) fwd_kernel(Args args) {
;     ...
;         int m = g4 ? (256 * (8 * (bx & 7) + ((bx >> 3) & 7)) + 64 * (bx >> 6) + 8 * wave) : gw;
;         const int step = g4 ? 1 : ngw, cnt = g4 ? 8 : (M - gw + ngw - 1) / ngw;
;         for (int i = 0; i < cnt; ++i, m += step) final_row(WSP(WS_H) + (size_t)m * D, (const float*)(ws + WS_SS) + (size_t)m * 32, gv, xo + (size_t)m * D, lane); }
.Lfin_first:
	v_readlane_b32 s2, v252, 4
	v_readlane_b32 s3, v252, 5
	s_nop 1
	v_lshl_add_u64 v[82:83], s[2:3], 0, v[50:51]
	v_add_co_u32_e32 v84, vcc, 0xb600000, v82
	s_nop 1
	v_addc_co_u32_e32 v85, vcc, 0, v83, vcc
	global_load_dwordx4 v[76:79], v[84:85], off
	global_load_dwordx4 v[72:75], v[84:85], off offset:1024
	global_load_dwordx4 v[68:71], v[84:85], off offset:2048
	global_load_dwordx4 v[64:67], v[84:85], off offset:3072
	v_mov_b32_e32 v80, 0
	s_and_saveexec_b64 s[2:3], s[0:1]
	s_cbranch_execz .Lfin_ld_a
	v_readlane_b32 s14, v252, 4
	v_readlane_b32 s15, v252, 5
	s_nop 1
	v_lshl_add_u64 v[84:85], s[14:15], 0, v[48:49]
	global_load_dword v80, v[84:85], off
.Lfin_ld_a:
	s_or_b64 exec, exec, s[2:3]
	s_waitcnt vmcnt(0)
	s_branch .Lfin_go
.Lfin_top:
	s_waitcnt vmcnt(8)
.Lfin_go:
	v_mov_b32_e32 v56, v80
	v_mov_b32_e32 v32, v64
	v_mov_b32_e32 v33, v65
	v_mov_b32_e32 v34, v66
	v_mov_b32_e32 v35, v67
	v_mov_b32_e32 v36, v68
	v_mov_b32_e32 v37, v69
	v_mov_b32_e32 v38, v70
	v_mov_b32_e32 v39, v71
	v_mov_b32_e32 v40, v72
	v_mov_b32_e32 v41, v73
	v_mov_b32_e32 v42, v74
	v_mov_b32_e32 v43, v75
	v_mov_b32_e32 v44, v76
	v_mov_b32_e32 v45, v77
	v_mov_b32_e32 v46, v78
	v_mov_b32_e32 v47, v79
	v_add_f32_dpp v56, v56, v56 quad_perm:[1,0,3,2] row_mask:0xf bank_mask:0xf bound_ctrl:1
	s_add_i32 s12, s12, -1
	v_lshl_add_u64 v[48:49], v[48:49], 0, s[4:5]
	v_add_f32_dpp v56, v56, v56 quad_perm:[2,3,0,1] row_mask:0xf bank_mask:0xf bound_ctrl:1
	v_lshl_add_u64 v[50:51], v[50:51], 0, s[6:7]
	s_cmp_eq_u32 s12, 0
	s_cbranch_scc1 .Lfin_noload
	v_readlane_b32 s2, v252, 4
	v_readlane_b32 s3, v252, 5
	s_nop 1
	v_lshl_add_u64 v[82:83], s[2:3], 0, v[50:51]
	v_add_co_u32_e32 v84, vcc, 0xb600000, v82
	s_nop 1
	v_addc_co_u32_e32 v85, vcc, 0, v83, vcc
	global_load_dwordx4 v[76:79], v[84:85], off
	global_load_dwordx4 v[72:75], v[84:85], off offset:1024
	global_load_dwordx4 v[68:71], v[84:85], off offset:2048
	global_load_dwordx4 v[64:67], v[84:85], off offset:3072
	v_mov_b32_e32 v80, 0
	s_and_saveexec_b64 s[2:3], s[0:1]
	s_cbranch_execz .Lfin_ld_b
	v_readlane_b32 s14, v252, 4
	v_readlane_b32 s15, v252, 5
	s_nop 1
	v_lshl_add_u64 v[84:85], s[14:15], 0, v[48:49]
	global_load_dword v80, v[84:85], off

; __device__ __forceinline__ float wave_sum(float v) { v += dpp_f<0xB1>(v); v += dpp_f<0x4E>(v); v += dpp_f<0x141>(v); v += dpp_f<0x140>(v); return sum_xor32(sum_xor16(v)); }
; __device__ __forceinline__ float bflo(unsigned w) { return __uint_as_float(w << 16); }
; __device__ __forceinline__ float bfhi(unsigned w) { return __uint_as_float(w & 0xffff0000u); }
; __device__ __forceinline__ void final_row(const bf16* hrow, const float* ss, const f32x4 (&gv)[8], float* orow, int lane) {
;     ...
;     const float s = wave_sum((lane < 32) ? ss[lane & 31] : 0.f);
;     const float rstd = 1.0f / sqrtf(s * (1.f / 2048.f) + EPS);
; #pragma unroll
;     for (int j = 0; j < 4; ++j) { float* op = orow + 8 * (lane + 64 * j);
;         *(f32x4*)op = (f32x4){bflo(h[j].x) * rstd * gv[2 * j].x, bfhi(h[j].x) * rstd * gv[2 * j].y, bflo(h[j].y) * rstd * gv[2 * j].z, bfhi(h[j].y) * rstd * gv[2 * j].w};
;         *(f32x4*)(op + 4) = (f32x4){bflo(h[j].z) * rstd * gv[2 * j + 1].x, bfhi(h[j].z) * rstd * gv[2 * j + 1].y, bflo(h[j].w) * rstd * gv[2 * j + 1].z, bfhi(h[j].w) * rstd * gv[2 * j + 1].w}; }
.Lfin_noload:
	v_add_f32_dpp v56, v56, v56 row_half_mirror row_mask:0xf bank_mask:0xf bound_ctrl:1
	s_nop 1
	v_add_f32_dpp v56, v56, v56 row_mirror row_mask:0xf bank_mask:0xf bound_ctrl:1
	v_mov_b32_e32 v57, v56
	s_nop 1
	v_permlane16_swap_b32_e32 v56, v57
	v_add_f32_e32 v56, v56, v57
	v_mov_b32_e32 v57, v56
	s_nop 1
	v_permlane32_swap_b32_e32 v56, v57
	v_add_f32_e32 v56, v56, v57
	v_fmamk_f32 v56, v56, 0x3a000000, v54
	v_mul_f32_e32 v57, 0x4f800000, v56
	v_cmp_gt_f32_e32 vcc, s10, v56
	s_nop 1
	v_cndmask_b32_e32 v56, v56, v57, vcc
	v_sqrt_f32_e32 v57, v56
	s_nop 0
	v_add_u32_e32 v58, -1, v57
	v_fma_f32 v59, -v58, v57, v56
	v_cmp_ge_f32_e64 s[2:3], 0, v59
	v_add_u32_e32 v59, 1, v57
	s_nop 0
	v_cndmask_b32_e64 v58, v57, v58, s[2:3]
	v_fma_f32 v57, -v59, v57, v56
	v_cmp_lt_f32_e64 s[2:3], 0, v57
	s_nop 1
	v_cndmask_b32_e64 v57, v58, v59, s[2:3]
	v_mul_f32_e32 v58, 0x37800000, v57
	v_cndmask_b32_e32 v57, v57, v58, vcc
	v_cmp_class_f32_e32 vcc, v56, v55
	s_nop 1
	v_cndmask_b32_e32 v56, v57, v56, vcc
	v_div_scale_f32 v57, s[2:3], v56, v56, 1.0
	v_rcp_f32_e32 v58, v57
	s_nop 0
	v_fma_f32 v59, -v57, v58, 1.0
	v_fmac_f32_e32 v58, v59, v58
	v_div_scale_f32 v59, vcc, 1.0, v56, 1.0
	v_mul_f32_e32 v60, v59, v58
	v_fma_f32 v61, -v57, v60, v59
	v_fmac_f32_e32 v60, v61, v58
	v_fma_f32 v57, -v57, v60, v59
	v_div_fmas_f32 v57, v57, v58, v60
	v_div_fixup_f32 v60, v57, v56, 1.0
	v_lshlrev_b32_e32 v56, 16, v44
	v_and_b32_e32 v57, 0xffff0000, v44
	v_lshlrev_b32_e32 v44, 16, v45
	v_and_b32_e32 v45, 0xffff0000, v45
	v_pk_mul_f32 v[44:45], v[60:61], v[44:45] op_sel_hi:[0,1]
	v_pk_mul_f32 v[58:59], v[6:7], v[44:45]
	v_lshlrev_b32_e32 v44, 16, v46
	v_and_b32_e32 v45, 0xffff0000, v46
	v_lshlrev_b32_e32 v46, 16, v47
	v_and_b32_e32 v47, 0xffff0000, v47
	v_pk_mul_f32 v[44:45], v[60:61], v[44:45] op_sel_hi:[0,1]
	v_pk_mul_f32 v[46:47], v[60:61], v[46:47] op_sel_hi:[0,1]
	v_pk_mul_f32 v[44:45], v[0:1], v[44:45]
	v_pk_mul_f32 v[46:47], v[2:3], v[46:47]
	global_store_dwordx4 v[52:53], v[44:47], off offset:-4080
	v_pk_mul_f32 v[56:57], v[60:61], v[56:57] op_sel_hi:[0,1]
	v_pk_mul_f32 v[56:57], v[4:5], v[56:57]
	v_lshlrev_b32_e32 v44, 16, v40
	v_and_b32_e32 v45, 0xffff0000, v40
	v_lshlrev_b32_e32 v40, 16, v41
	v_and_b32_e32 v41, 0xffff0000, v41
	v_pk_mul_f32 v[40:41], v[60:61], v[40:41] op_sel_hi:[0,1]
	v_pk_mul_f32 v[46:47], v[14:15], v[40:41]
	v_lshlrev_b32_e32 v40, 16, v42
	v_and_b32_e32 v41, 0xffff0000, v42
	v_lshlrev_b32_e32 v42, 16, v43
	v_and_b32_e32 v43, 0xffff0000, v43
	v_pk_mul_f32 v[40:41], v[60:61], v[40:41] op_sel_hi:[0,1]
	v_pk_mul_f32 v[42:43], v[60:61], v[42:43] op_sel_hi:[0,1]
	v_pk_mul_f32 v[40:41], v[8:9], v[40:41]
	v_pk_mul_f32 v[42:43], v[10:11], v[42:43]
	global_store_dwordx4 v[52:53], v[40:43], off offset:-2032
	v_pk_mul_f32 v[44:45], v[60:61], v[44:45] op_sel_hi:[0,1]
	v_pk_mul_f32 v[44:45], v[12:13], v[44:45]
	v_lshlrev_b32_e32 v40, 16, v36
	v_and_b32_e32 v41, 0xffff0000, v36
	v_lshlrev_b32_e32 v36, 16, v37
	v_and_b32_e32 v37, 0xffff0000, v37
	v_pk_mul_f32 v[36:37], v[60:61], v[36:37] op_sel_hi:[0,1]
	v_pk_mul_f32 v[42:43], v[22:23], v[36:37]
	v_lshlrev_b32_e32 v36, 16, v38
	v_and_b32_e32 v37, 0xffff0000, v38
	v_lshlrev_b32_e32 v38, 16, v39
	v_and_b32_e32 v39, 0xffff0000, v39
	v_pk_mul_f32 v[36:37], v[60:61], v[36:37] op_sel_hi:[0,1]
	v_pk_mul_f32 v[38:39], v[60:61], v[38:39] op_sel_hi:[0,1]
	v_pk_mul_f32 v[36:37], v[16:17], v[36:37]
	v_pk_mul_f32 v[38:39], v[18:19], v[38:39]
	global_store_dwordx4 v[52:53], v[36:39], off offset:16
	v_pk_mul_f32 v[40:41], v[60:61], v[40:41] op_sel_hi:[0,1]
	v_pk_mul_f32 v[40:41], v[20:21], v[40:41]
	v_lshlrev_b32_e32 v36, 16, v32
	v_and_b32_e32 v37, 0xffff0000, v32
	v_lshlrev_b32_e32 v32, 16, v33
	v_and_b32_e32 v33, 0xffff0000, v33
	v_pk_mul_f32 v[32:33], v[60:61], v[32:33] op_sel_hi:[0,1]
	v_pk_mul_f32 v[38:39], v[30:31], v[32:33]
	v_lshlrev_b32_e32 v32, 16, v34
	v_and_b32_e32 v33, 0xffff0000, v34
	v_lshlrev_b32_e32 v34, 16, v35
	v_and_b32_e32 v35, 0xffff0000, v35
	v_pk_mul_f32 v[36:37], v[60:61], v[36:37] op_sel_hi:[0,1]
	v_pk_mul_f32 v[32:33], v[60:61], v[32:33] op_sel_hi:[0,1]
	v_pk_mul_f32 v[34:35], v[60:61], v[34:35] op_sel_hi:[0,1]
	v_pk_mul_f32 v[36:37], v[28:29], v[36:37]
	v_pk_mul_f32 v[32:33], v[24:25], v[32:33]
	v_pk_mul_f32 v[34:35], v[26:27], v[34:35]
	global_store_dwordx4 v[52:53], v[56:59], off offset:-4096
	global_store_dwordx4 v[52:53], v[44:47], off offset:-2048
	global_store_dwordx4 v[52:53], v[40:43], off
	global_store_dwordx4 v[52:53], v[36:39], off offset:2048
	global_store_dwordx4 v[52:53], v[32:35], off offset:2064
	v_lshl_add_u64 v[52:53], v[52:53], 0, s[8:9]
	s_cmp_eq_u32 s12, 0
	s_cbranch_scc1 .LBB0_1789
	s_branch .Lfin_top
